# plus chunk-C output loop unrolled x4 with the four output-gate row loads issued up front
# speedup vs baseline: 1.0013x; 1.0013x over previous
.LBB0_1087:
	v_ashrrev_i32_e32 v20, 5, v1
	v_add_u32_e32 v18, s74, v20
	v_and_b32_e32 v10, 0xf8, v0
	v_mov_b64_e32 v[6:7], s[30:31]
	v_lshlrev_b32_e32 v136, 1, v10
	v_mad_i64_i32 v[6:7], s[60:61], v18, s83, v[6:7]
	v_lshl_add_u64 v[218:219], v[6:7], 0, v[136:137]
	v_lshlrev_b32_e32 v14, 2, v10
	global_load_dwordx4 v[10:13], v14, s[6:7] offset:16
	s_nop 0
	global_load_dwordx4 v[14:17], v14, s[6:7]
	s_mov_b64 s[60:61], 0x32000
	global_load_dwordx4 v[6:9], v[218:219], off
	v_lshl_add_u64 v[220:221], v[218:219], 0, s[60:61]
	global_load_dwordx4 v[204:207], v[220:221], off
	v_lshl_add_u64 v[220:221], v[220:221], 0, s[60:61]
	global_load_dwordx4 v[208:211], v[220:221], off
	v_lshl_add_u64 v[220:221], v[220:221], 0, s[60:61]
	global_load_dwordx4 v[212:215], v[220:221], off
	v_mul_lo_u32 v2, v20, s87
	s_add_i32 s4, 0, 0x18800
	v_add3_u32 v216, s4, v2, v136
	v_lshl_add_u32 v20, v20, 2, 0
	v_add_u32_e32 v217, 0x13900, v20
	v_ashrrev_i32_e32 v19, 31, v18
	s_waitcnt vmcnt(3)
	ds_read_b128 v[2:5], v216
	ds_read_b32 v20, v217
	v_lshlrev_b32_e32 v21, 16, v6
	v_mul_f32_e32 v22, 0xbfb8aa3b, v21
	v_exp_f32_e32 v22, v22
	v_and_b32_e32 v6, 0xffff0000, v6
	v_add_f32_e32 v22, 1.0, v22
	v_rcp_f32_e32 v22, v22
	s_nop 0
	v_mul_f32_e32 v21, v22, v21
	v_cndmask_b32_e64 v21, v21, v22, s[90:91]
	v_mul_f32_e32 v22, 0xbfb8aa3b, v6
	v_exp_f32_e32 v22, v22
	s_nop 0
	v_add_f32_e32 v22, 1.0, v22
	v_rcp_f32_e32 v22, v22
	s_nop 0
	v_mul_f32_e32 v6, v22, v6
	v_cndmask_b32_e64 v6, v6, v22, s[90:91]
	s_waitcnt lgkmcnt(1)
	v_lshlrev_b32_e32 v22, 16, v2
	v_and_b32_e32 v2, 0xffff0000, v2
	s_waitcnt lgkmcnt(0)
	v_mul_f32_e32 v2, v20, v2
	v_mul_f32_e32 v22, v20, v22
	v_mul_f32_e32 v2, v2, v6
	v_lshlrev_b32_e32 v6, 16, v7
	v_mul_f32_e32 v21, v22, v21
	v_mul_f32_e32 v22, 0xbfb8aa3b, v6
	v_exp_f32_e32 v22, v22
	v_and_b32_e32 v7, 0xffff0000, v7
	v_mul_f32_e32 v2, v15, v2
	v_add_f32_e32 v22, 1.0, v22
	v_rcp_f32_e32 v22, v22
	s_nop 0
	v_mul_f32_e32 v6, v22, v6
	v_cndmask_b32_e64 v6, v6, v22, s[90:91]
	v_mul_f32_e32 v22, 0xbfb8aa3b, v7
	v_exp_f32_e32 v22, v22
	s_nop 0
	v_add_f32_e32 v22, 1.0, v22
	v_rcp_f32_e32 v22, v22
	s_nop 0
	v_mul_f32_e32 v7, v22, v7
	v_cndmask_b32_e64 v7, v7, v22, s[90:91]
	v_lshlrev_b32_e32 v22, 16, v3
	v_and_b32_e32 v3, 0xffff0000, v3
	v_mul_f32_e32 v3, v20, v3
	v_mul_f32_e32 v22, v20, v22
	v_mul_f32_e32 v3, v3, v7
	v_lshlrev_b32_e32 v7, 16, v8
	v_mul_f32_e32 v6, v22, v6
	v_mul_f32_e32 v22, 0xbfb8aa3b, v7
	v_exp_f32_e32 v22, v22
	v_and_b32_e32 v8, 0xffff0000, v8
	v_mul_f32_e32 v6, v16, v6
	v_mul_f32_e32 v3, v17, v3
	v_add_f32_e32 v22, 1.0, v22
	v_rcp_f32_e32 v22, v22
	v_cvt_pk_bf16_f32 v3, v6, v3
	v_mul_f32_e32 v7, v22, v7
	v_cndmask_b32_e64 v7, v7, v22, s[90:91]
	v_mul_f32_e32 v22, 0xbfb8aa3b, v8
	v_exp_f32_e32 v22, v22
	s_nop 0
	v_add_f32_e32 v22, 1.0, v22
	v_rcp_f32_e32 v22, v22
	s_nop 0
	v_mul_f32_e32 v8, v22, v8
	v_cndmask_b32_e64 v8, v8, v22, s[90:91]
	v_lshlrev_b32_e32 v22, 16, v4
	v_and_b32_e32 v4, 0xffff0000, v4
	v_mul_f32_e32 v4, v20, v4
	v_mul_f32_e32 v22, v20, v22
	v_mul_f32_e32 v4, v4, v8
	v_lshlrev_b32_e32 v8, 16, v9
	v_mul_f32_e32 v7, v22, v7
	v_mul_f32_e32 v22, 0xbfb8aa3b, v8
	v_exp_f32_e32 v22, v22
	v_and_b32_e32 v9, 0xffff0000, v9
	v_mul_f32_e32 v6, v10, v7
	v_mul_f32_e32 v4, v11, v4
	v_add_f32_e32 v22, 1.0, v22
	v_rcp_f32_e32 v22, v22
	v_cvt_pk_bf16_f32 v4, v6, v4
	v_mul_f32_e32 v8, v22, v8
	v_cndmask_b32_e64 v8, v8, v22, s[90:91]
	v_mul_f32_e32 v22, 0xbfb8aa3b, v9
	v_exp_f32_e32 v22, v22
	s_nop 0
	v_add_f32_e32 v22, 1.0, v22
	v_rcp_f32_e32 v22, v22
	s_nop 0
	v_mul_f32_e32 v9, v22, v9
	v_cndmask_b32_e64 v9, v9, v22, s[90:91]
	v_lshlrev_b32_e32 v22, 16, v5
	v_and_b32_e32 v5, 0xffff0000, v5
	v_mul_f32_e32 v22, v20, v22
	v_mul_f32_e32 v5, v20, v5
	v_mul_f32_e32 v8, v22, v8
	v_mul_f32_e32 v5, v5, v9
	v_mul_f32_e32 v6, v12, v8
	v_mul_f32_e32 v5, v13, v5
	v_cvt_pk_bf16_f32 v5, v6, v5
	v_lshlrev_b64 v[6:7], 12, v[18:19]
	v_mul_f32_e32 v9, v14, v21
	v_lshl_add_u64 v[6:7], s[36:37], 0, v[6:7]
	v_cvt_pk_bf16_f32 v2, v9, v2
	v_lshl_add_u64 v[6:7], v[6:7], 0, v[136:137]
	global_store_dwordx4 v[6:7], v[2:5], off
	s_nop 1
	s_waitcnt vmcnt(3)
	v_mov_b32_e32 v6, v204
	v_mov_b32_e32 v7, v205
	v_mov_b32_e32 v8, v206
	v_mov_b32_e32 v9, v207
	v_add_u32_e32 v18, 16, v18
	ds_read_b128 v[2:5], v216 offset:8448
	ds_read_b32 v20, v217 offset:64
	v_lshlrev_b32_e32 v21, 16, v6
	v_mul_f32_e32 v22, 0xbfb8aa3b, v21
	v_exp_f32_e32 v22, v22
	v_and_b32_e32 v6, 0xffff0000, v6
	v_add_f32_e32 v22, 1.0, v22
	v_rcp_f32_e32 v22, v22
	s_nop 0
	v_mul_f32_e32 v21, v22, v21
	v_cndmask_b32_e64 v21, v21, v22, s[90:91]
	v_mul_f32_e32 v22, 0xbfb8aa3b, v6
	v_exp_f32_e32 v22, v22
	s_nop 0
	v_add_f32_e32 v22, 1.0, v22
	v_rcp_f32_e32 v22, v22
	s_nop 0
	v_mul_f32_e32 v6, v22, v6
	v_cndmask_b32_e64 v6, v6, v22, s[90:91]
	s_waitcnt lgkmcnt(1)
	v_lshlrev_b32_e32 v22, 16, v2
	v_and_b32_e32 v2, 0xffff0000, v2
	s_waitcnt lgkmcnt(0)
	v_mul_f32_e32 v2, v20, v2
	v_mul_f32_e32 v22, v20, v22
	v_mul_f32_e32 v2, v2, v6
	v_lshlrev_b32_e32 v6, 16, v7
	v_mul_f32_e32 v21, v22, v21
	v_mul_f32_e32 v22, 0xbfb8aa3b, v6
	v_exp_f32_e32 v22, v22
	v_and_b32_e32 v7, 0xffff0000, v7
	v_mul_f32_e32 v2, v15, v2
	v_add_f32_e32 v22, 1.0, v22
	v_rcp_f32_e32 v22, v22
	s_nop 0
	v_mul_f32_e32 v6, v22, v6
	v_cndmask_b32_e64 v6, v6, v22, s[90:91]
	v_mul_f32_e32 v22, 0xbfb8aa3b, v7
	v_exp_f32_e32 v22, v22
	s_nop 0
	v_add_f32_e32 v22, 1.0, v22
	v_rcp_f32_e32 v22, v22
	s_nop 0
	v_mul_f32_e32 v7, v22, v7
	v_cndmask_b32_e64 v7, v7, v22, s[90:91]
	v_lshlrev_b32_e32 v22, 16, v3
	v_and_b32_e32 v3, 0xffff0000, v3
	v_mul_f32_e32 v3, v20, v3
	v_mul_f32_e32 v22, v20, v22
	v_mul_f32_e32 v3, v3, v7
	v_lshlrev_b32_e32 v7, 16, v8
	v_mul_f32_e32 v6, v22, v6
	v_mul_f32_e32 v22, 0xbfb8aa3b, v7
	v_exp_f32_e32 v22, v22
	v_and_b32_e32 v8, 0xffff0000, v8
	v_mul_f32_e32 v6, v16, v6
	v_mul_f32_e32 v3, v17, v3
	v_add_f32_e32 v22, 1.0, v22
	v_rcp_f32_e32 v22, v22
	v_cvt_pk_bf16_f32 v3, v6, v3
	v_mul_f32_e32 v7, v22, v7
	v_cndmask_b32_e64 v7, v7, v22, s[90:91]
	v_mul_f32_e32 v22, 0xbfb8aa3b, v8
	v_exp_f32_e32 v22, v22
	s_nop 0
	v_add_f32_e32 v22, 1.0, v22
	v_rcp_f32_e32 v22, v22
	s_nop 0
	v_mul_f32_e32 v8, v22, v8
	v_cndmask_b32_e64 v8, v8, v22, s[90:91]
	v_lshlrev_b32_e32 v22, 16, v4
	v_and_b32_e32 v4, 0xffff0000, v4
	v_mul_f32_e32 v4, v20, v4
	v_mul_f32_e32 v22, v20, v22
	v_mul_f32_e32 v4, v4, v8
	v_lshlrev_b32_e32 v8, 16, v9
	v_mul_f32_e32 v7, v22, v7
	v_mul_f32_e32 v22, 0xbfb8aa3b, v8
	v_exp_f32_e32 v22, v22
	v_and_b32_e32 v9, 0xffff0000, v9
	v_mul_f32_e32 v6, v10, v7
	v_mul_f32_e32 v4, v11, v4
	v_add_f32_e32 v22, 1.0, v22
	v_rcp_f32_e32 v22, v22
	v_cvt_pk_bf16_f32 v4, v6, v4
	v_mul_f32_e32 v8, v22, v8
	v_cndmask_b32_e64 v8, v8, v22, s[90:91]
	v_mul_f32_e32 v22, 0xbfb8aa3b, v9
	v_exp_f32_e32 v22, v22
	s_nop 0
	v_add_f32_e32 v22, 1.0, v22
	v_rcp_f32_e32 v22, v22
	s_nop 0
	v_mul_f32_e32 v9, v22, v9
	v_cndmask_b32_e64 v9, v9, v22, s[90:91]
	v_lshlrev_b32_e32 v22, 16, v5
	v_and_b32_e32 v5, 0xffff0000, v5
	v_mul_f32_e32 v22, v20, v22
	v_mul_f32_e32 v5, v20, v5
	v_mul_f32_e32 v8, v22, v8
	v_mul_f32_e32 v5, v5, v9
	v_mul_f32_e32 v6, v12, v8
	v_mul_f32_e32 v5, v13, v5
	v_cvt_pk_bf16_f32 v5, v6, v5
	v_lshlrev_b64 v[6:7], 12, v[18:19]
	v_mul_f32_e32 v9, v14, v21
	v_lshl_add_u64 v[6:7], s[36:37], 0, v[6:7]
	v_cvt_pk_bf16_f32 v2, v9, v2
	v_lshl_add_u64 v[6:7], v[6:7], 0, v[136:137]
	global_store_dwordx4 v[6:7], v[2:5], off
	s_nop 1
	s_waitcnt vmcnt(3)
	v_mov_b32_e32 v6, v208
	v_mov_b32_e32 v7, v209
	v_mov_b32_e32 v8, v210
	v_mov_b32_e32 v9, v211
	v_add_u32_e32 v18, 16, v18
	ds_read_b128 v[2:5], v216 offset:16896
	ds_read_b32 v20, v217 offset:128
	v_lshlrev_b32_e32 v21, 16, v6
	v_mul_f32_e32 v22, 0xbfb8aa3b, v21
	v_exp_f32_e32 v22, v22
	v_and_b32_e32 v6, 0xffff0000, v6
	v_add_f32_e32 v22, 1.0, v22
	v_rcp_f32_e32 v22, v22
	s_nop 0
	v_mul_f32_e32 v21, v22, v21
	v_cndmask_b32_e64 v21, v21, v22, s[90:91]
	v_mul_f32_e32 v22, 0xbfb8aa3b, v6
	v_exp_f32_e32 v22, v22
	s_nop 0
	v_add_f32_e32 v22, 1.0, v22
	v_rcp_f32_e32 v22, v22
	s_nop 0
	v_mul_f32_e32 v6, v22, v6
	v_cndmask_b32_e64 v6, v6, v22, s[90:91]
	s_waitcnt lgkmcnt(1)
	v_lshlrev_b32_e32 v22, 16, v2
	v_and_b32_e32 v2, 0xffff0000, v2
	s_waitcnt lgkmcnt(0)
	v_mul_f32_e32 v2, v20, v2
	v_mul_f32_e32 v22, v20, v22
	v_mul_f32_e32 v2, v2, v6
	v_lshlrev_b32_e32 v6, 16, v7
	v_mul_f32_e32 v21, v22, v21
	v_mul_f32_e32 v22, 0xbfb8aa3b, v6
	v_exp_f32_e32 v22, v22
	v_and_b32_e32 v7, 0xffff0000, v7
	v_mul_f32_e32 v2, v15, v2
	v_add_f32_e32 v22, 1.0, v22
	v_rcp_f32_e32 v22, v22
	s_nop 0
	v_mul_f32_e32 v6, v22, v6
	v_cndmask_b32_e64 v6, v6, v22, s[90:91]
	v_mul_f32_e32 v22, 0xbfb8aa3b, v7
	v_exp_f32_e32 v22, v22
	s_nop 0
	v_add_f32_e32 v22, 1.0, v22
	v_rcp_f32_e32 v22, v22
	s_nop 0
	v_mul_f32_e32 v7, v22, v7
	v_cndmask_b32_e64 v7, v7, v22, s[90:91]
	v_lshlrev_b32_e32 v22, 16, v3
	v_and_b32_e32 v3, 0xffff0000, v3
	v_mul_f32_e32 v3, v20, v3
	v_mul_f32_e32 v22, v20, v22
	v_mul_f32_e32 v3, v3, v7
	v_lshlrev_b32_e32 v7, 16, v8
	v_mul_f32_e32 v6, v22, v6
	v_mul_f32_e32 v22, 0xbfb8aa3b, v7
	v_exp_f32_e32 v22, v22
	v_and_b32_e32 v8, 0xffff0000, v8
	v_mul_f32_e32 v6, v16, v6
	v_mul_f32_e32 v3, v17, v3
	v_add_f32_e32 v22, 1.0, v22
	v_rcp_f32_e32 v22, v22
	v_cvt_pk_bf16_f32 v3, v6, v3
	v_mul_f32_e32 v7, v22, v7
	v_cndmask_b32_e64 v7, v7, v22, s[90:91]
	v_mul_f32_e32 v22, 0xbfb8aa3b, v8
	v_exp_f32_e32 v22, v22
	s_nop 0
	v_add_f32_e32 v22, 1.0, v22
	v_rcp_f32_e32 v22, v22
	s_nop 0
	v_mul_f32_e32 v8, v22, v8
	v_cndmask_b32_e64 v8, v8, v22, s[90:91]
	v_lshlrev_b32_e32 v22, 16, v4
	v_and_b32_e32 v4, 0xffff0000, v4
	v_mul_f32_e32 v4, v20, v4
	v_mul_f32_e32 v22, v20, v22
	v_mul_f32_e32 v4, v4, v8
	v_lshlrev_b32_e32 v8, 16, v9
	v_mul_f32_e32 v7, v22, v7
	v_mul_f32_e32 v22, 0xbfb8aa3b, v8
	v_exp_f32_e32 v22, v22
	v_and_b32_e32 v9, 0xffff0000, v9
	v_mul_f32_e32 v6, v10, v7
	v_mul_f32_e32 v4, v11, v4
	v_add_f32_e32 v22, 1.0, v22
	v_rcp_f32_e32 v22, v22
	v_cvt_pk_bf16_f32 v4, v6, v4
	v_mul_f32_e32 v8, v22, v8
	v_cndmask_b32_e64 v8, v8, v22, s[90:91]
	v_mul_f32_e32 v22, 0xbfb8aa3b, v9
	v_exp_f32_e32 v22, v22
	s_nop 0
	v_add_f32_e32 v22, 1.0, v22
	v_rcp_f32_e32 v22, v22
	s_nop 0
	v_mul_f32_e32 v9, v22, v9
	v_cndmask_b32_e64 v9, v9, v22, s[90:91]
	v_lshlrev_b32_e32 v22, 16, v5
	v_and_b32_e32 v5, 0xffff0000, v5
	v_mul_f32_e32 v22, v20, v22
	v_mul_f32_e32 v5, v20, v5
	v_mul_f32_e32 v8, v22, v8
	v_mul_f32_e32 v5, v5, v9
	v_mul_f32_e32 v6, v12, v8
	v_mul_f32_e32 v5, v13, v5
	v_cvt_pk_bf16_f32 v5, v6, v5
	v_lshlrev_b64 v[6:7], 12, v[18:19]
	v_mul_f32_e32 v9, v14, v21
	v_lshl_add_u64 v[6:7], s[36:37], 0, v[6:7]
	v_cvt_pk_bf16_f32 v2, v9, v2
	v_lshl_add_u64 v[6:7], v[6:7], 0, v[136:137]
	global_store_dwordx4 v[6:7], v[2:5], off
	s_nop 1
	s_waitcnt vmcnt(3)
	v_mov_b32_e32 v6, v212
	v_mov_b32_e32 v7, v213
	v_mov_b32_e32 v8, v214
	v_mov_b32_e32 v9, v215
	v_add_u32_e32 v18, 16, v18
	ds_read_b128 v[2:5], v216 offset:25344
	ds_read_b32 v20, v217 offset:192
	v_lshlrev_b32_e32 v21, 16, v6
	v_mul_f32_e32 v22, 0xbfb8aa3b, v21
	v_exp_f32_e32 v22, v22
	v_and_b32_e32 v6, 0xffff0000, v6
	v_add_f32_e32 v22, 1.0, v22
	v_rcp_f32_e32 v22, v22
	s_nop 0
	v_mul_f32_e32 v21, v22, v21
	v_cndmask_b32_e64 v21, v21, v22, s[90:91]
	v_mul_f32_e32 v22, 0xbfb8aa3b, v6
	v_exp_f32_e32 v22, v22
	s_nop 0
	v_add_f32_e32 v22, 1.0, v22
	v_rcp_f32_e32 v22, v22
	s_nop 0
	v_mul_f32_e32 v6, v22, v6
	v_cndmask_b32_e64 v6, v6, v22, s[90:91]
	s_waitcnt lgkmcnt(1)
	v_lshlrev_b32_e32 v22, 16, v2
	v_and_b32_e32 v2, 0xffff0000, v2
	s_waitcnt lgkmcnt(0)
	v_mul_f32_e32 v2, v20, v2
	v_mul_f32_e32 v22, v20, v22
	v_mul_f32_e32 v2, v2, v6
	v_lshlrev_b32_e32 v6, 16, v7
	v_mul_f32_e32 v21, v22, v21
	v_mul_f32_e32 v22, 0xbfb8aa3b, v6
	v_exp_f32_e32 v22, v22
	v_and_b32_e32 v7, 0xffff0000, v7
	v_mul_f32_e32 v2, v15, v2
	v_add_f32_e32 v22, 1.0, v22
	v_rcp_f32_e32 v22, v22
	s_nop 0
	v_mul_f32_e32 v6, v22, v6
	v_cndmask_b32_e64 v6, v6, v22, s[90:91]
	v_mul_f32_e32 v22, 0xbfb8aa3b, v7
	v_exp_f32_e32 v22, v22
	s_nop 0
	v_add_f32_e32 v22, 1.0, v22
	v_rcp_f32_e32 v22, v22
	s_nop 0
	v_mul_f32_e32 v7, v22, v7
	v_cndmask_b32_e64 v7, v7, v22, s[90:91]
	v_lshlrev_b32_e32 v22, 16, v3
	v_and_b32_e32 v3, 0xffff0000, v3
	v_mul_f32_e32 v3, v20, v3
	v_mul_f32_e32 v22, v20, v22
	v_mul_f32_e32 v3, v3, v7
	v_lshlrev_b32_e32 v7, 16, v8
	v_mul_f32_e32 v6, v22, v6
	v_mul_f32_e32 v22, 0xbfb8aa3b, v7
	v_exp_f32_e32 v22, v22
	v_and_b32_e32 v8, 0xffff0000, v8
	v_mul_f32_e32 v6, v16, v6
	v_mul_f32_e32 v3, v17, v3
	v_add_f32_e32 v22, 1.0, v22
	v_rcp_f32_e32 v22, v22
	v_cvt_pk_bf16_f32 v3, v6, v3
	v_mul_f32_e32 v7, v22, v7
	v_cndmask_b32_e64 v7, v7, v22, s[90:91]
	v_mul_f32_e32 v22, 0xbfb8aa3b, v8
	v_exp_f32_e32 v22, v22
	s_nop 0
	v_add_f32_e32 v22, 1.0, v22
	v_rcp_f32_e32 v22, v22
	s_nop 0
	v_mul_f32_e32 v8, v22, v8
	v_cndmask_b32_e64 v8, v8, v22, s[90:91]
	v_lshlrev_b32_e32 v22, 16, v4
	v_and_b32_e32 v4, 0xffff0000, v4
	v_mul_f32_e32 v4, v20, v4
	v_mul_f32_e32 v22, v20, v22
	v_mul_f32_e32 v4, v4, v8
	v_lshlrev_b32_e32 v8, 16, v9
	v_mul_f32_e32 v7, v22, v7
	v_mul_f32_e32 v22, 0xbfb8aa3b, v8
	v_exp_f32_e32 v22, v22
	v_and_b32_e32 v9, 0xffff0000, v9
	v_mul_f32_e32 v6, v10, v7
	v_mul_f32_e32 v4, v11, v4
	v_add_f32_e32 v22, 1.0, v22
	v_rcp_f32_e32 v22, v22
	v_cvt_pk_bf16_f32 v4, v6, v4
	v_mul_f32_e32 v8, v22, v8
	v_cndmask_b32_e64 v8, v8, v22, s[90:91]
	v_mul_f32_e32 v22, 0xbfb8aa3b, v9
	v_exp_f32_e32 v22, v22
	s_nop 0
	v_add_f32_e32 v22, 1.0, v22
	v_rcp_f32_e32 v22, v22
	s_nop 0
	v_mul_f32_e32 v9, v22, v9
	v_cndmask_b32_e64 v9, v9, v22, s[90:91]
	v_lshlrev_b32_e32 v22, 16, v5
	v_and_b32_e32 v5, 0xffff0000, v5
	v_mul_f32_e32 v22, v20, v22
	v_mul_f32_e32 v5, v20, v5
	v_mul_f32_e32 v8, v22, v8
	v_mul_f32_e32 v5, v5, v9
	v_mul_f32_e32 v6, v12, v8
	v_mul_f32_e32 v5, v13, v5
	v_cvt_pk_bf16_f32 v5, v6, v5
	v_lshlrev_b64 v[6:7], 12, v[18:19]
	v_mul_f32_e32 v9, v14, v21
	v_lshl_add_u64 v[6:7], s[36:37], 0, v[6:7]
	v_cvt_pk_bf16_f32 v2, v9, v2
	v_lshl_add_u64 v[6:7], v[6:7], 0, v[136:137]
	global_store_dwordx4 v[6:7], v[2:5], off
	s_nop 1
	s_branch .LBB0_949
